# gla_c and tr work queues: next ticket requested during the current item's tail (after its last vmcnt wait) and only collected at the loop head; first gla_c ticket requested at the top of the setup cod
# speedup vs baseline: 1.0019x; 1.0019x over previous
.LBB0_1053:
	s_nop 0
	s_nop 0
	s_nop 0
	s_nop 0
	v_and_b32_e32 v3, 64, v68
	v_xor_b32_e32 v2, 32, v68
	v_add_u32_e32 v3, 64, v3
	v_cmp_lt_i32_e32 vcc, v2, v3
	s_mov_b64 s[20:21], -1
	s_mov_b64 s[22:23], -1
	v_cndmask_b32_e32 v2, v68, v2, vcc
	v_lshlrev_b32_e32 v2, 2, v2
	ds_bpermute_b32 v6, v2, v71
	ds_bpermute_b32 v5, v2, v50
	ds_bpermute_b32 v3, v2, v57
	ds_bpermute_b32 v7, v2, v69
	ds_bpermute_b32 v4, v2, v59
	ds_bpermute_b32 v2, v2, v70
	s_waitcnt lgkmcnt(5)
	v_cmp_nlt_f32_e32 vcc, v71, v6
	s_and_saveexec_b64 s[18:19], vcc
	s_cbranch_execz .LBB0_1057
	v_cmp_eq_f32_e32 vcc, v71, v6
	s_mov_b64 s[22:23], 0
	s_and_saveexec_b64 s[24:25], vcc
	s_cbranch_execz .LBB0_1056
	s_waitcnt lgkmcnt(2)
	v_cmp_lt_i32_e32 vcc, v7, v69
	s_and_b64 s[22:23], vcc, exec

.LBB0_1410:
	s_and_saveexec_b64 s[98:99], s[40:41]
	v_mov_b32_e32 v2, 0
	v_mov_b32_e32 v231, 1
	global_atomic_add v231, v2, v231, s[46:47] offset:256 sc0
	s_mov_b64 exec, s[98:99]
	s_lshl_b32 s0, s91, 5
	v_lshlrev_b32_e32 v2, 6, v0
	v_or_b32_e32 v130, s0, v156
	v_and_b32_e32 v2, 0x800, v2
	v_add_u32_e32 v132, v130, v2
	v_lshlrev_b32_e32 v2, 3, v0
	s_waitcnt lgkmcnt(0)
	v_or_b32_e32 v4, 0x400, v0
	v_lshrrev_b32_e32 v173, 6, v4
	v_lshrrev_b32_e32 v8, 5, v0
	v_lshrrev_b32_e32 v181, 5, v4
	v_and_b32_e32 v4, 0xc0, v2
	v_or_b32_e32 v3, 0x200, v0
	v_or_b32_e32 v8, v4, v8
	v_and_b32_e32 v2, 56, v2
	s_movk_i32 s1, 0x48
	v_lshrrev_b32_e32 v180, 5, v3
	v_mad_u32_u24 v8, v8, s1, v2
	v_or_b32_e32 v5, 0x600, v0
	v_lshl_add_u32 v183, v8, 1, 0
	v_or_b32_e32 v8, v4, v180
	v_lshrrev_b32_e32 v182, 5, v5
	v_mad_u32_u24 v8, v8, s1, v2
	v_lshl_add_u32 v184, v8, 1, 0
	v_or_b32_e32 v8, v4, v181
	v_or_b32_e32 v4, v4, v182
	v_mad_u32_u24 v8, v8, s1, v2
	v_mad_u32_u24 v2, v4, s1, v2
	v_lshl_add_u32 v186, v2, 1, 0
	v_lshlrev_b32_e32 v2, 10, v0
	v_lshrrev_b32_e32 v10, 4, v0
	v_lshrrev_b32_e32 v172, 6, v3
	v_and_b32_e32 v2, 0xc000, v2
	s_add_i32 s6, 0, 0x13800
	v_and_b32_e32 v4, 15, v0
	v_and_b32_e32 v10, 12, v10
	v_lshrrev_b32_e32 v3, 8, v3
	v_add_u32_e32 v2, s6, v2
	v_bitop3_b32 v3, v10, v4, v3 bitop3:0x36
	v_lshl_add_u32 v12, v3, 4, v2
	v_bfe_u32 v3, v5, 8, 2
	v_or_b32_e32 v6, 0xa00, v0
	v_bitop3_b32 v3, v10, v4, v3 bitop3:0x36
	v_lshl_add_u32 v15, v3, 4, v2
	v_bfe_u32 v3, v6, 8, 2
	v_or_b32_e32 v7, 0xe00, v0
	v_bitop3_b32 v3, v10, v4, v3 bitop3:0x36
	v_lshl_add_u32 v18, v3, 4, v2
	v_bfe_u32 v3, v7, 8, 2
	v_lshrrev_b32_e32 v9, 8, v0
	v_bitop3_b32 v3, v10, v4, v3 bitop3:0x36
	v_lshrrev_b32_e32 v174, 6, v5
	v_bitop3_b32 v9, v10, v4, v9 bitop3:0x36
	v_lshl_add_u32 v10, v3, 4, v2
	v_lshlrev_b32_e32 v3, 4, v0
	v_lshrrev_b32_e32 v5, 2, v0
	v_lshrrev_b32_e32 v176, 6, v6
	v_lshl_add_u32 v9, v9, 4, v2
	v_and_b32_e32 v2, 0x1f0, v3
	v_and_b32_e32 v6, 8, v5
	v_lshlrev_b32_e32 v4, 2, v2
	v_lshlrev_b32_e32 v5, 2, v6
	v_lshrrev_b32_e32 v178, 6, v7
	v_add3_u32 v187, 0, v4, v5
	v_lshrrev_b32_e32 v7, 3, v0
	v_mov_b32_e32 v5, 0x1fffffc4
	v_and_or_b32 v4, s0, 32, v156
	v_bitop3_b32 v5, s0, v5, v7 bitop3:0xc8
	v_mov_b32_e32 v135, 0
	v_mad_u64_u32 v[4:5], s[0:1], v5, s1, v[4:5]
	v_lshlrev_b32_e32 v134, 1, v6
	v_lshl_add_u32 v188, v4, 1, 0
	v_lshl_add_u64 v[4:5], s[44:45], 0, v[134:135]
	v_lshlrev_b32_e32 v134, 7, v156
	v_lshl_add_u64 v[4:5], v[4:5], 0, v[134:135]
	s_mov_b64 s[0:1], 0x3000000
	v_lshl_add_u64 v[142:143], v[4:5], 0, s[0:1]
	s_lshr_b32 s0, s74, 8
	s_xor_b32 s0, s0, s91
	s_lshr_b32 s49, s74, 7
	s_and_b32 s0, s0, 1
	s_lshl_b32 s1, s49, 6
	s_lshl_b32 s7, s0, 5
	s_or_b32 s1, s7, s1
	v_or_b32_e32 v4, s1, v156
	s_movk_i32 s33, 0x90
	v_mul_lo_u32 v4, v4, s33
	v_add_u32_e32 v5, 0, v4
	v_bfe_u32 v4, v0, 1, 1
	v_and_or_b32 v7, v7, 2, v4
	v_lshlrev_b32_e32 v4, 3, v248
	v_and_b32_e32 v24, 8, v4
	v_lshlrev_b32_e32 v4, 2, v157
	v_or_b32_e32 v25, 2, v4
	v_cmp_gt_u32_e64 s[10:11], v25, v156
	v_or_b32_e32 v25, 3, v4
	v_cmp_gt_u32_e64 s[12:13], v25, v156
	v_or_b32_e32 v25, 8, v4
	v_cmp_gt_u32_e64 s[14:15], v25, v156
	v_or_b32_e32 v25, 9, v4
	v_cmp_gt_u32_e64 s[16:17], v25, v156
	v_or_b32_e32 v25, 10, v4
	v_cmp_gt_u32_e64 s[18:19], v25, v156
	v_or_b32_e32 v25, 11, v4
	v_cmp_gt_u32_e64 s[20:21], v25, v156
	v_or_b32_e32 v25, 16, v4
	v_cmp_gt_u32_e64 s[22:23], v25, v156
	v_or_b32_e32 v25, 17, v4
	v_cmp_gt_u32_e64 s[24:25], v25, v156
	v_or_b32_e32 v25, 18, v4
	v_cmp_gt_u32_e64 s[26:27], v25, v156
	v_or_b32_e32 v25, 19, v4
	v_cmp_gt_u32_e64 s[28:29], v25, v156
	v_or_b32_e32 v25, 24, v4
	v_cmp_gt_u32_e64 s[30:31], v25, v156
	v_or_b32_e32 v25, 25, v4
	v_bfe_u32 v22, v0, 2, 2
	v_cmp_gt_u32_e64 s[34:35], v25, v156
	v_or_b32_e32 v25, 26, v4
	v_lshlrev_b32_e32 v23, 2, v22
	v_cmp_gt_u32_e64 s[36:37], v25, v156
	v_or_b32_e32 v25, 27, v4
	v_bfe_u32 v47, v0, 5, 1
	v_or_b32_e32 v6, v23, v157
	v_cmp_gt_u32_e64 s[38:39], v25, v156
	v_bitop3_b32 v25, v23, v7, v157 bitop3:0x36
	v_or_b32_e32 v23, v47, v23
	v_or_b32_e32 v26, 4, v7
	v_bitop3_b32 v27, v7, v6, 4 bitop3:0x36
	v_or_b32_e32 v28, 8, v7
	v_bitop3_b32 v29, v7, v6, 8 bitop3:0x36
	v_or_b32_e32 v30, 12, v7
	v_bitop3_b32 v6, v7, v6, 12 bitop3:0x36
	v_bitop3_b32 v7, v23, v7, 2 bitop3:0x36
	v_lshlrev_b32_e32 v48, 4, v7
	v_bitop3_b32 v7, v23, v26, 2 bitop3:0x36
	s_lshl_b32 s54, s49, 14
	v_lshlrev_b32_e32 v26, 4, v7
	v_bitop3_b32 v7, v23, v28, 2 bitop3:0x36
	s_add_i32 s1, s6, s54
	s_lshl_b32 s78, s0, 13
	v_lshlrev_b32_e32 v134, 4, v248
	v_lshlrev_b32_e32 v28, 4, v7
	v_bitop3_b32 v7, v23, v30, 2 bitop3:0x36
	v_lshlrev_b32_e32 v31, 4, v6
	v_lshlrev_b32_e32 v32, 8, v156
	v_lshlrev_b32_e32 v6, 2, v0
	s_add_i32 s1, s1, s78
	v_lshlrev_b32_e32 v34, 3, v157
	v_lshl_add_u64 v[144:145], s[70:71], 0, v[134:135]
	v_lshlrev_b32_e32 v23, 4, v7
	v_and_b32_e32 v134, 0x3f0, v3
	v_mov_b32_e32 v3, v135
	v_mov_b32_e32 v7, v135
	v_add3_u32 v189, s1, v32, v34
	v_lshl_add_u64 v[150:151], s[66:67], 0, v[2:3]
	v_lshl_add_u64 v[2:3], s[46:47], 0, v[6:7]
	s_mov_b64 s[0:1], 0x1c10000
	v_lshl_add_u64 v[152:153], v[2:3], 0, s[0:1]
	v_lshlrev_b32_e32 v2, 10, v47
	v_lshlrev_b32_e32 v3, 8, v22
	v_or3_b32 v2, s54, v2, v3
	v_or3_b32 v3, v2, v48, v24
	v_add_u32_e32 v3, 0, v3
	v_lshlrev_b32_e32 v29, 4, v29
	v_add_u32_e32 v193, 0x15000, v3
	v_add_u32_e32 v197, 0x14000, v3
	v_or3_b32 v3, v2, v31, v24
	v_lshlrev_b32_e32 v25, 4, v25
	v_lshlrev_b32_e32 v27, 4, v27
	v_add_u32_e32 v201, 0, v3
	v_or3_b32 v3, v2, v29, v24
	v_and_or_b32 v33, v6, 12, v22
	v_add_u32_e32 v192, 0, v6
	v_or3_b32 v6, v2, v26, v24
	v_or3_b32 v7, v2, v28, v24
	v_or3_b32 v22, v2, v23, v24
	v_add_u32_e32 v202, 0, v3
	v_or3_b32 v3, v2, v27, v24
	v_or3_b32 v2, v2, v25, v24
	s_mul_i32 s0, s49, 0x2400
	v_lshrrev_b32_e32 v167, 6, v0
	v_add_u32_e32 v204, 0, v2
	v_mov_b32_e32 v2, s0
	v_or_b32_e32 v16, 32, v167
	v_or_b32_e32 v19, 48, v167
	v_lshlrev_b32_e32 v21, 4, v157
	v_lshlrev_b32_e32 v190, 4, v33
	v_mad_u32_u24 v2, v156, s33, v2
	v_add_u32_e32 v136, 0x400, v132
	v_add_u32_e32 v138, 0x500, v132
	v_add_u32_e32 v140, 0x600, v132
	v_lshl_add_u32 v185, v8, 1, 0
	v_lshlrev_b32_e32 v8, 8, v167
	v_lshlrev_b32_e32 v11, 8, v172
	v_lshlrev_b32_e32 v13, 8, v173
	v_lshlrev_b32_e32 v14, 8, v174
	v_lshlrev_b32_e32 v16, 8, v16
	v_lshlrev_b32_e32 v17, 8, v176
	v_lshlrev_b32_e32 v19, 8, v19
	v_lshlrev_b32_e32 v20, 8, v178
	v_xor_b32_e32 v32, 16, v190
	v_xor_b32_e32 v33, 32, v190
	v_xor_b32_e32 v34, 48, v190
	v_xor_b32_e32 v35, 64, v190
	v_xor_b32_e32 v36, 0x50, v190
	v_xor_b32_e32 v37, 0x60, v190
	v_xor_b32_e32 v38, 0x70, v190
	v_xor_b32_e32 v39, 0x80, v190
	v_xor_b32_e32 v40, 0x90, v190
	v_xor_b32_e32 v41, 0xa0, v190
	v_xor_b32_e32 v42, 0xb0, v190
	v_xor_b32_e32 v43, 0xc0, v190
	v_xor_b32_e32 v44, 0xd0, v190
	v_xor_b32_e32 v45, 0xe0, v190
	v_xor_b32_e32 v46, 0xf0, v190
	v_add_u32_e32 v6, 0, v6
	v_add_u32_e32 v7, 0, v7
	v_add_u32_e32 v22, 0, v22
	v_add3_u32 v2, v2, v21, 0
	v_mov_b32_e32 v133, v135
	v_ashrrev_i32_e32 v137, 31, v136
	v_ashrrev_i32_e32 v139, 31, v138
	v_ashrrev_i32_e32 v141, 31, v140
	v_mov_b32_e32 v131, v135
	v_cmp_gt_u32_e64 s[4:5], 32, v248
	v_writelane_b32 v255, s74, 4
	v_cmp_gt_u32_e64 s[6:7], v4, v156
	v_cmp_lt_u32_e64 s[8:9], v4, v156
	v_ashrrev_i32_e32 v147, 31, v132
	v_mov_b32_e32 v146, v132
	v_lshl_add_u64 v[148:149], s[66:67], 0, v[134:135]
	v_add_u32_e32 v194, 0x15000, v6
	v_add_u32_e32 v195, 0x15000, v7
	v_add_u32_e32 v196, 0x15000, v22
	v_add_u32_e32 v198, 0x14000, v6
	v_add_u32_e32 v199, 0x14000, v7
	v_add_u32_e32 v200, 0x14000, v22
	v_add_u32_e32 v203, 0, v3
	v_add_u32_e32 v205, 0xa800, v2
	s_add_i32 s79, s78, 0x2000
	s_add_i32 s80, 0, 0x27e50
	s_add_i32 s81, 0, 0x27ea8
	s_add_i32 s82, 0, 0x27eac
	s_movk_i32 s83, 0x1000
	s_add_i32 s84, 0, 0x27eb0
	s_add_i32 s85, 0, 0x27eb4
	s_movk_i32 s92, 0xc00
	s_mov_b32 s93, 0xbfb8aa3b
	s_mov_b32 s94, 0x800000
	s_mov_b32 s95, 0x3f317217
	s_mov_b32 s96, 0x7f800000
	s_movk_i32 s97, 0x7fff
	v_add_u32_e32 v206, v5, v21
	s_add_i32 s54, 0, 0x27eb8
	s_add_i32 s55, 0, 0x27ebc
	v_lshlrev_b32_e32 v134, 2, v4
	v_add_u32_e32 v252, v189, v32
	v_add_u32_e32 v253, v189, v33
	v_add_u32_e32 v254, v189, v34
	v_add_u32_e32 v166, v189, v35
	v_add_u32_e32 v191, v189, v36
	v_add_u32_e32 v207, v189, v37
	v_add_u32_e32 v175, v189, v38
	v_add_u32_e32 v177, v189, v39
	v_add_u32_e32 v216, v189, v40
	v_add_u32_e32 v217, v189, v41
	v_add_u32_e32 v218, v189, v42
	v_add_u32_e32 v219, v189, v43
	v_add_u32_e32 v220, v189, v44
	v_add_u32_e32 v221, v189, v45
	v_add_u32_e32 v222, v189, v46
	v_add_u32_e32 v223, v9, v8
	v_add_u32_e32 v224, v12, v11
	v_add_u32_e32 v225, v9, v13
	v_add_u32_e32 v226, v15, v14
	v_add_u32_e32 v227, v9, v16
	v_add_u32_e32 v228, v18, v17
	v_add_u32_e32 v229, v9, v19
	v_add_u32_e32 v230, v10, v20
	s_branch .LBB0_1413
.LBB0_1411:
	v_mov_b32_e32 v66, s54
	v_mov_b32_e32 v67, s55
	ds_read_b32 v66, v66
	ds_read_b32 v67, v67
	s_waitcnt lgkmcnt(0)
	s_barrier
	s_waitcnt lgkmcnt(1)
	v_readfirstlane_b32 s0, v66
	s_waitcnt lgkmcnt(0)
	v_readfirstlane_b32 s1, v67
	v_mul_f32_e32 v80, v51, v51
	v_fmac_f32_e32 v80, v50, v50
	v_lshl_add_u64 v[68:69], s[0:1], 0, v[134:135]
	global_load_dwordx4 v[70:73], v[68:69], off
	global_load_dwordx4 v[114:117], v[68:69], off offset:32
	global_load_dwordx4 v[118:121], v[68:69], off offset:64
	global_load_dwordx4 v[122:125], v[68:69], off offset:96
	global_load_dwordx4 v[126:129], v[68:69], off offset:128
	global_load_dwordx4 v[208:211], v[68:69], off offset:160
	global_load_dwordx4 v[212:215], v[68:69], off offset:192
	global_load_dwordx4 v[232:235], v[68:69], off offset:224
	global_load_dwordx4 v[236:239], v[68:69], off offset:256
	global_load_dwordx4 v[240:243], v[68:69], off offset:288
	global_load_dwordx4 v[244:247], v[68:69], off offset:320
	global_load_dwordx4 v[248:251], v[68:69], off offset:384
	v_fmac_f32_e32 v80, v52, v52
	v_fmac_f32_e32 v80, v53, v53
	v_fmac_f32_e32 v80, v54, v54
	v_fmac_f32_e32 v80, v55, v55
	v_fmac_f32_e32 v80, v56, v56
	v_fmac_f32_e32 v80, v57, v57
	v_fmac_f32_e32 v80, v58, v58
	v_fmac_f32_e32 v80, v59, v59
	v_fmac_f32_e32 v80, v60, v60
	v_fmac_f32_e32 v80, v61, v61
	v_fmac_f32_e32 v80, v62, v62
	v_fmac_f32_e32 v80, v63, v63
	v_fmac_f32_e32 v80, v64, v64
	v_fmac_f32_e32 v80, v65, v65
	v_fmac_f32_e32 v80, v34, v34
	v_fmac_f32_e32 v80, v35, v35
	v_fmac_f32_e32 v80, v36, v36
	v_fmac_f32_e32 v80, v37, v37
	v_fmac_f32_e32 v80, v38, v38
	v_fmac_f32_e32 v80, v39, v39
	v_fmac_f32_e32 v80, v40, v40
	v_fmac_f32_e32 v80, v41, v41
	v_fmac_f32_e32 v80, v42, v42
	v_fmac_f32_e32 v80, v43, v43
	v_fmac_f32_e32 v80, v44, v44
	v_fmac_f32_e32 v80, v45, v45
	v_fmac_f32_e32 v80, v46, v46
	v_fmac_f32_e32 v80, v47, v47
	v_fmac_f32_e32 v80, v48, v48
	v_fmac_f32_e32 v80, v49, v49
	v_fmac_f32_e32 v80, v18, v18
	v_fmac_f32_e32 v80, v19, v19
	v_fmac_f32_e32 v80, v20, v20
	v_fmac_f32_e32 v80, v21, v21
	v_fmac_f32_e32 v80, v22, v22
	v_fmac_f32_e32 v80, v23, v23
	v_fmac_f32_e32 v80, v24, v24
	v_fmac_f32_e32 v80, v25, v25
	v_fmac_f32_e32 v80, v26, v26
	v_fmac_f32_e32 v80, v27, v27
	v_fmac_f32_e32 v80, v28, v28
	v_fmac_f32_e32 v80, v29, v29
	v_fmac_f32_e32 v80, v30, v30
	v_fmac_f32_e32 v80, v31, v31
	v_fmac_f32_e32 v80, v32, v32
	v_fmac_f32_e32 v80, v33, v33
	v_fmac_f32_e32 v80, v2, v2
	v_fmac_f32_e32 v80, v3, v3
	v_fmac_f32_e32 v80, v4, v4
	v_fmac_f32_e32 v80, v5, v5
	v_fmac_f32_e32 v80, v6, v6
	v_fmac_f32_e32 v80, v7, v7
	v_fmac_f32_e32 v80, v8, v8
	v_fmac_f32_e32 v80, v9, v9
	v_pk_mul_f32 v[78:79], v[10:11], v[10:11]
	v_pk_mul_f32 v[76:77], v[12:13], v[12:13]
	v_add_f32_e32 v78, v78, v80
	v_add_f32_e32 v78, v79, v78
	v_add_f32_e32 v76, v76, v78
	v_pk_mul_f32 v[74:75], v[14:15], v[14:15]
	v_add_f32_e32 v76, v77, v76
	v_add_f32_e32 v74, v74, v76
	v_pk_mul_f32 v[66:67], v[16:17], v[16:17]
	v_add_f32_e32 v74, v75, v74
	v_add_f32_e32 v66, v66, v74
	v_add_f32_e32 v66, v67, v66
	ds_bpermute_b32 v67, v1, v66
	s_waitcnt vmcnt(0)
	v_lshlrev_b32_e32 v76, 16, v91
	v_and_b32_e32 v77, 0xffff0000, v91
	v_lshlrev_b32_e32 v78, 16, v92
	v_and_b32_e32 v79, 0xffff0000, v92
	s_waitcnt lgkmcnt(0)
	v_add_f32_e32 v66, v66, v67
	v_mov_b32_e32 v67, 0x358637bd
	v_fmamk_f32 v66, v66, 0x3c000000, v67
	v_rsq_f32_e32 v66, v66
	v_add_u32_e32 v67, v189, v190
	v_lshlrev_b32_e32 v80, 16, v93
	v_and_b32_e32 v81, 0xffff0000, v93
	v_pk_mul_f32 v[50:51], v[50:51], v[66:67] op_sel_hi:[1,0]
	v_pk_mul_f32 v[52:53], v[52:53], v[66:67] op_sel_hi:[1,0]
	v_pk_mul_f32 v[50:51], v[50:51], v[70:71]
	v_pk_mul_f32 v[52:53], v[52:53], v[72:73]
	v_cvt_pk_bf16_f32 v50, v50, v51
	v_cvt_pk_bf16_f32 v51, v52, v53
	ds_write_b64 v67, v[50:51]
	v_pk_mul_f32 v[54:55], v[54:55], v[66:67] op_sel_hi:[1,0]
	v_pk_mul_f32 v[56:57], v[56:57], v[66:67] op_sel_hi:[1,0]
	v_pk_mul_f32 v[54:55], v[54:55], v[114:115]
	v_pk_mul_f32 v[56:57], v[56:57], v[116:117]
	v_cvt_pk_bf16_f32 v54, v54, v55
	v_cvt_pk_bf16_f32 v55, v56, v57
	ds_write_b64 v252, v[54:55]
	v_pk_mul_f32 v[58:59], v[58:59], v[66:67] op_sel_hi:[1,0]
	v_pk_mul_f32 v[60:61], v[60:61], v[66:67] op_sel_hi:[1,0]
	v_pk_mul_f32 v[58:59], v[58:59], v[118:119]
	v_pk_mul_f32 v[60:61], v[60:61], v[120:121]
	v_cvt_pk_bf16_f32 v58, v58, v59
	v_cvt_pk_bf16_f32 v59, v60, v61
	ds_write_b64 v253, v[58:59]
	v_pk_mul_f32 v[62:63], v[62:63], v[66:67] op_sel_hi:[1,0]
	v_pk_mul_f32 v[64:65], v[64:65], v[66:67] op_sel_hi:[1,0]
	v_pk_mul_f32 v[62:63], v[62:63], v[122:123]
	v_pk_mul_f32 v[64:65], v[64:65], v[124:125]
	v_cvt_pk_bf16_f32 v62, v62, v63
	v_cvt_pk_bf16_f32 v63, v64, v65
	ds_write_b64 v254, v[62:63]
	global_load_dwordx4 v[50:53], v[68:69], off offset:352
	global_load_dwordx4 v[54:57], v[68:69], off offset:416
	global_load_dwordx4 v[58:61], v[68:69], off offset:448
	global_load_dwordx4 v[62:65], v[68:69], off offset:480
	v_pk_mul_f32 v[34:35], v[34:35], v[66:67] op_sel_hi:[1,0]
	v_pk_mul_f32 v[36:37], v[36:37], v[66:67] op_sel_hi:[1,0]
	v_pk_mul_f32 v[34:35], v[34:35], v[126:127]
	v_pk_mul_f32 v[36:37], v[36:37], v[128:129]
	v_cvt_pk_bf16_f32 v34, v34, v35
	v_cvt_pk_bf16_f32 v35, v36, v37
	ds_write_b64 v166, v[34:35]
	v_pk_mul_f32 v[38:39], v[38:39], v[66:67] op_sel_hi:[1,0]
	v_pk_mul_f32 v[40:41], v[40:41], v[66:67] op_sel_hi:[1,0]
	v_pk_mul_f32 v[38:39], v[38:39], v[208:209]
	v_pk_mul_f32 v[40:41], v[40:41], v[210:211]
	v_cvt_pk_bf16_f32 v38, v38, v39
	v_cvt_pk_bf16_f32 v39, v40, v41
	ds_write_b64 v191, v[38:39]
	v_pk_mul_f32 v[42:43], v[42:43], v[66:67] op_sel_hi:[1,0]
	v_pk_mul_f32 v[44:45], v[44:45], v[66:67] op_sel_hi:[1,0]
	v_pk_mul_f32 v[42:43], v[42:43], v[212:213]
	v_pk_mul_f32 v[44:45], v[44:45], v[214:215]
	v_cvt_pk_bf16_f32 v42, v42, v43
	v_cvt_pk_bf16_f32 v43, v44, v45
	ds_write_b64 v207, v[42:43]
	v_pk_mul_f32 v[46:47], v[46:47], v[66:67] op_sel_hi:[1,0]
	v_pk_mul_f32 v[48:49], v[48:49], v[66:67] op_sel_hi:[1,0]
	v_pk_mul_f32 v[46:47], v[46:47], v[232:233]
	v_pk_mul_f32 v[48:49], v[48:49], v[234:235]
	v_cvt_pk_bf16_f32 v46, v46, v47
	v_cvt_pk_bf16_f32 v47, v48, v49
	ds_write_b64 v175, v[46:47]
	v_pk_mul_f32 v[18:19], v[18:19], v[66:67] op_sel_hi:[1,0]
	v_pk_mul_f32 v[20:21], v[20:21], v[66:67] op_sel_hi:[1,0]
	v_pk_mul_f32 v[18:19], v[18:19], v[236:237]
	v_pk_mul_f32 v[20:21], v[20:21], v[238:239]
	v_cvt_pk_bf16_f32 v18, v18, v19
	v_cvt_pk_bf16_f32 v19, v20, v21
	ds_write_b64 v177, v[18:19]
	v_pk_mul_f32 v[22:23], v[22:23], v[66:67] op_sel_hi:[1,0]
	v_pk_mul_f32 v[24:25], v[24:25], v[66:67] op_sel_hi:[1,0]
	v_pk_mul_f32 v[22:23], v[22:23], v[240:241]
	v_pk_mul_f32 v[24:25], v[24:25], v[242:243]
	v_cvt_pk_bf16_f32 v22, v22, v23
	v_cvt_pk_bf16_f32 v23, v24, v25
	ds_write_b64 v216, v[22:23]
	v_pk_mul_f32 v[26:27], v[26:27], v[66:67] op_sel_hi:[1,0]
	v_pk_mul_f32 v[28:29], v[28:29], v[66:67] op_sel_hi:[1,0]
	v_pk_mul_f32 v[26:27], v[26:27], v[244:245]
	v_pk_mul_f32 v[28:29], v[28:29], v[246:247]
	v_cvt_pk_bf16_f32 v26, v26, v27
	v_cvt_pk_bf16_f32 v27, v28, v29
	ds_write_b64 v217, v[26:27]
	v_pk_mul_f32 v[2:3], v[2:3], v[66:67] op_sel_hi:[1,0]
	v_pk_mul_f32 v[4:5], v[4:5], v[66:67] op_sel_hi:[1,0]
	v_pk_mul_f32 v[2:3], v[2:3], v[248:249]
	v_pk_mul_f32 v[4:5], v[4:5], v[250:251]
	v_cvt_pk_bf16_f32 v2, v2, v3
	v_cvt_pk_bf16_f32 v3, v4, v5
	ds_write_b64 v219, v[2:3]
	s_waitcnt vmcnt(0)
	s_and_saveexec_b64 s[98:99], s[40:41]
	v_mov_b32_e32 v231, 1
	global_atomic_add v231, v135, v231, s[46:47] offset:256 sc0
	s_mov_b64 exec, s[98:99]
	v_pk_mul_f32 v[30:31], v[30:31], v[66:67] op_sel_hi:[1,0]
	v_pk_mul_f32 v[32:33], v[32:33], v[66:67] op_sel_hi:[1,0]
	v_pk_mul_f32 v[30:31], v[30:31], v[50:51]
	v_pk_mul_f32 v[32:33], v[32:33], v[52:53]
	v_cvt_pk_bf16_f32 v30, v30, v31
	v_cvt_pk_bf16_f32 v31, v32, v33
	ds_write_b64 v218, v[30:31]
	v_pk_mul_f32 v[6:7], v[6:7], v[66:67] op_sel_hi:[1,0]
	v_pk_mul_f32 v[8:9], v[8:9], v[66:67] op_sel_hi:[1,0]
	v_pk_mul_f32 v[6:7], v[6:7], v[54:55]
	v_pk_mul_f32 v[8:9], v[8:9], v[56:57]
	v_cvt_pk_bf16_f32 v6, v6, v7
	v_cvt_pk_bf16_f32 v7, v8, v9
	ds_write_b64 v220, v[6:7]
	v_pk_mul_f32 v[10:11], v[10:11], v[66:67] op_sel_hi:[1,0]
	v_pk_mul_f32 v[12:13], v[12:13], v[66:67] op_sel_hi:[1,0]
	v_pk_mul_f32 v[10:11], v[10:11], v[58:59]
	v_pk_mul_f32 v[12:13], v[12:13], v[60:61]
	v_cvt_pk_bf16_f32 v10, v10, v11
	v_cvt_pk_bf16_f32 v11, v12, v13
	ds_write_b64 v221, v[10:11]
	v_pk_mul_f32 v[14:15], v[14:15], v[66:67] op_sel_hi:[1,0]
	v_pk_mul_f32 v[16:17], v[16:17], v[66:67] op_sel_hi:[1,0]
	v_pk_mul_f32 v[14:15], v[14:15], v[62:63]
	v_pk_mul_f32 v[16:17], v[16:17], v[64:65]
	v_cvt_pk_bf16_f32 v14, v14, v15
	v_cvt_pk_bf16_f32 v15, v16, v17
	ds_write_b64 v222, v[14:15]
	v_lshlrev_b32_e32 v70, 16, v97
	v_and_b32_e32 v71, 0xffff0000, v97
	v_lshlrev_b32_e32 v72, 16, v90
	v_and_b32_e32 v73, 0xffff0000, v90
	v_lshlrev_b32_e32 v90, 16, v86
	v_and_b32_e32 v91, 0xffff0000, v86
	v_lshlrev_b32_e32 v86, 16, v87
	v_and_b32_e32 v87, 0xffff0000, v87
	v_lshlrev_b32_e32 v92, 16, v88
	v_and_b32_e32 v93, 0xffff0000, v88
	v_lshlrev_b32_e32 v88, 16, v89
	v_and_b32_e32 v89, 0xffff0000, v89
	v_and_b32_e32 v97, 0xffff0000, v83
	v_lshlrev_b64 v[74:75], 11, v[168:169]
	v_lshlrev_b64 v[114:115], 11, v[154:155]
	v_mul_f32_e32 v213, 0xbfb8aa3b, v70
	v_mul_f32_e32 v214, 0xbfb8aa3b, v71
	v_mul_f32_e32 v215, 0xbfb8aa3b, v72
	v_mul_f32_e32 v232, 0xbfb8aa3b, v73
	v_mul_f32_e32 v233, 0xbfb8aa3b, v76
	v_mul_f32_e32 v234, 0xbfb8aa3b, v77
	v_mul_f32_e32 v235, 0xbfb8aa3b, v78
	v_mul_f32_e32 v236, 0xbfb8aa3b, v79
	v_mul_f32_e32 v237, 0xbfb8aa3b, v80
	v_mul_f32_e32 v238, 0xbfb8aa3b, v81
	v_mul_f32_e32 v239, 0xbfb8aa3b, v86
	v_mul_f32_e32 v240, 0xbfb8aa3b, v87
	v_mul_f32_e32 v241, 0xbfb8aa3b, v92
	v_mul_f32_e32 v242, 0xbfb8aa3b, v93
	v_mul_f32_e32 v243, 0xbfb8aa3b, v88
	v_mul_f32_e32 v244, 0xbfb8aa3b, v89
	s_mov_b64 s[0:1], 0
	v_lshlrev_b64 v[60:61], 11, v[170:171]
	v_lshlrev_b32_e32 v58, 16, v94
	v_and_b32_e32 v59, 0xffff0000, v94
	v_lshlrev_b32_e32 v94, 16, v82
	v_lshlrev_b32_e32 v62, 16, v95
	v_and_b32_e32 v63, 0xffff0000, v95
	v_lshlrev_b32_e32 v64, 16, v96
	v_and_b32_e32 v65, 0xffff0000, v96
	v_lshlrev_b32_e32 v96, 16, v83
	v_mul_f32_e32 v209, 0xbfb8aa3b, v62
	v_mul_f32_e32 v210, 0xbfb8aa3b, v63
	v_mul_f32_e32 v211, 0xbfb8aa3b, v64
	v_mul_f32_e32 v212, 0xbfb8aa3b, v65
	v_and_b32_e32 v95, 0xffff0000, v82
	v_lshlrev_b32_e32 v54, 16, v100
	v_and_b32_e32 v55, 0xffff0000, v100
	v_lshlrev_b32_e32 v56, 16, v101
	v_and_b32_e32 v57, 0xffff0000, v101
	v_mul_f32_e32 v169, 0xbfb8aa3b, v54
	v_mul_f32_e32 v170, 0xbfb8aa3b, v55
	v_mul_f32_e32 v171, 0xbfb8aa3b, v56
	v_mul_f32_e32 v208, 0xbfb8aa3b, v57
	v_lshlrev_b32_e32 v100, 16, v84
	v_and_b32_e32 v101, 0xffff0000, v84
	v_lshlrev_b32_e32 v84, 16, v85
	v_and_b32_e32 v85, 0xffff0000, v85
	v_lshlrev_b32_e32 v50, 16, v98
	v_and_b32_e32 v51, 0xffff0000, v98
	v_lshlrev_b32_e32 v52, 16, v99
	v_and_b32_e32 v53, 0xffff0000, v99
	v_lshlrev_b64 v[98:99], 11, v[162:163]
	v_mul_f32_e32 v163, 0xbfb8aa3b, v50
	v_mul_f32_e32 v168, 0xbfb8aa3b, v53
	v_lshlrev_b32_e32 v42, 16, v102
	v_and_b32_e32 v43, 0xffff0000, v102
	v_lshlrev_b32_e32 v44, 16, v103
	v_and_b32_e32 v45, 0xffff0000, v103
	v_lshlrev_b64 v[102:103], 11, v[164:165]
	v_mul_f32_e32 v155, 0xbfb8aa3b, v42
	v_mul_f32_e32 v164, 0xbfb8aa3b, v51
	v_mul_f32_e32 v165, 0xbfb8aa3b, v52
	v_lshlrev_b32_e32 v46, 16, v104
	v_and_b32_e32 v47, 0xffff0000, v104
	v_lshlrev_b32_e32 v48, 16, v105
	v_and_b32_e32 v49, 0xffff0000, v105
	v_lshlrev_b64 v[104:105], 11, v[160:161]
	v_mul_f32_e32 v160, 0xbfb8aa3b, v47
	v_mul_f32_e32 v161, 0xbfb8aa3b, v48
	v_mul_f32_e32 v162, 0xbfb8aa3b, v49
	v_lshlrev_b32_e32 v38, 16, v108
	v_and_b32_e32 v39, 0xffff0000, v108
	v_lshlrev_b32_e32 v40, 16, v109
	v_and_b32_e32 v41, 0xffff0000, v109
	v_mul_f32_e32 v127, 0xbfb8aa3b, v38
	v_mul_f32_e32 v128, 0xbfb8aa3b, v39
	v_mul_f32_e32 v129, 0xbfb8aa3b, v40
	v_mul_f32_e32 v154, 0xbfb8aa3b, v41
	v_lshlrev_b32_e32 v34, 16, v106
	v_and_b32_e32 v35, 0xffff0000, v106
	v_lshlrev_b32_e32 v36, 16, v107
	v_and_b32_e32 v37, 0xffff0000, v107
	v_mul_f32_e32 v123, 0xbfb8aa3b, v34
	v_mul_f32_e32 v124, 0xbfb8aa3b, v35
	v_mul_f32_e32 v125, 0xbfb8aa3b, v36
	v_mul_f32_e32 v126, 0xbfb8aa3b, v37
	v_lshlrev_b32_e32 v26, 16, v112
	v_and_b32_e32 v27, 0xffff0000, v112
	v_lshlrev_b32_e32 v28, 16, v113
	v_and_b32_e32 v29, 0xffff0000, v113
	v_lshlrev_b64 v[112:113], 11, v[156:157]
	v_mul_f32_e32 v119, 0xbfb8aa3b, v26
	v_mul_f32_e32 v120, 0xbfb8aa3b, v27
	v_mul_f32_e32 v121, 0xbfb8aa3b, v28
	v_mul_f32_e32 v122, 0xbfb8aa3b, v29
	v_mul_f32_e32 v156, 0xbfb8aa3b, v43
	v_mul_f32_e32 v157, 0xbfb8aa3b, v44
	v_lshl_add_u64 v[82:83], v[144:145], 0, v[112:113]
	v_mul_f32_e32 v112, 0xbfb8aa3b, v94
	v_mul_f32_e32 v113, 0xbfb8aa3b, v95
	v_exp_f32_e32 v112, v112
	v_exp_f32_e32 v113, v113
	v_add_f32_e32 v247, 1.0, v112
	v_add_f32_e32 v248, 1.0, v113
	v_lshlrev_b32_e32 v22, 16, v110
	v_mul_f32_e32 v67, 0xbfb8aa3b, v22
	v_exp_f32_e32 v67, v67
	v_and_b32_e32 v23, 0xffff0000, v110
	v_lshlrev_b32_e32 v24, 16, v111
	v_and_b32_e32 v25, 0xffff0000, v111
	v_lshlrev_b64 v[110:111], 11, v[158:159]
	v_mul_f32_e32 v116, 0xbfb8aa3b, v23
	v_mul_f32_e32 v117, 0xbfb8aa3b, v24
	v_mul_f32_e32 v118, 0xbfb8aa3b, v25
	v_mul_f32_e32 v158, 0xbfb8aa3b, v45
	v_mul_f32_e32 v159, 0xbfb8aa3b, v46
	v_add_f32_e32 v67, 1.0, v67
	v_lshl_add_u64 v[18:19], v[144:145], 0, v[60:61]
	v_lshl_add_u64 v[30:31], v[144:145], 0, v[102:103]
	v_lshl_add_u64 v[60:61], v[144:145], 0, v[104:105]
	v_lshl_add_u64 v[20:21], v[144:145], 0, v[74:75]
	v_lshl_add_u64 v[32:33], v[144:145], 0, v[98:99]
	v_mul_f32_e32 v98, 0xbfb8aa3b, v58
	v_mul_f32_e32 v99, 0xbfb8aa3b, v59
	v_lshl_add_u64 v[74:75], v[144:145], 0, v[110:111]
	v_mul_f32_e32 v110, 0xbfb8aa3b, v90
	v_mul_f32_e32 v111, 0xbfb8aa3b, v91
	v_exp_f32_e32 v98, v98
	v_exp_f32_e32 v99, v99
	v_exp_f32_e32 v110, v110
	v_exp_f32_e32 v111, v111
	v_add_f32_e32 v245, 1.0, v110
	v_add_f32_e32 v246, 1.0, v111
	v_mul_f32_e32 v4, 0xbfb8aa3b, v96
	v_mul_f32_e32 v5, 0xbfb8aa3b, v97
	v_lshl_add_u64 v[2:3], v[144:145], 0, v[114:115]
	v_exp_f32_e32 v114, v116
	v_exp_f32_e32 v115, v117
	v_exp_f32_e32 v116, v118
	v_exp_f32_e32 v117, v119
	v_exp_f32_e32 v118, v120
	v_exp_f32_e32 v119, v121
	v_exp_f32_e32 v120, v122
	v_exp_f32_e32 v121, v123
	v_exp_f32_e32 v122, v124
	v_exp_f32_e32 v123, v125
	v_exp_f32_e32 v124, v126
	v_exp_f32_e32 v125, v127
	v_exp_f32_e32 v126, v128
	v_exp_f32_e32 v127, v129
	v_exp_f32_e32 v128, v154
	v_exp_f32_e32 v129, v155
	v_exp_f32_e32 v154, v156
	v_exp_f32_e32 v155, v157
	v_exp_f32_e32 v156, v158
	v_exp_f32_e32 v157, v159
	v_exp_f32_e32 v158, v160
	v_exp_f32_e32 v159, v161
	v_exp_f32_e32 v160, v162
	v_exp_f32_e32 v161, v163
	v_exp_f32_e32 v162, v164
	v_exp_f32_e32 v163, v165
	v_exp_f32_e32 v164, v168
	v_exp_f32_e32 v165, v169
	v_exp_f32_e32 v168, v170
	v_exp_f32_e32 v169, v171
	v_exp_f32_e32 v170, v208
	v_exp_f32_e32 v171, v209
	v_exp_f32_e32 v208, v210
	v_exp_f32_e32 v209, v211
	v_exp_f32_e32 v210, v212
	v_exp_f32_e32 v211, v213
	v_exp_f32_e32 v212, v214
	v_exp_f32_e32 v213, v215
	v_exp_f32_e32 v214, v232
	v_exp_f32_e32 v215, v233
	v_exp_f32_e32 v232, v234
	v_exp_f32_e32 v233, v235
	v_exp_f32_e32 v234, v236
	v_exp_f32_e32 v235, v237
	v_exp_f32_e32 v236, v238
	v_exp_f32_e32 v237, v239
	v_exp_f32_e32 v238, v240
	v_exp_f32_e32 v239, v241
	v_exp_f32_e32 v240, v242
	v_exp_f32_e32 v241, v243
	v_exp_f32_e32 v242, v244
	v_exp_f32_e32 v243, v4
	v_exp_f32_e32 v244, v5
	v_mul_f32_e32 v106, 0xbfb8aa3b, v100
	v_add_f32_e32 v114, 1.0, v114
	v_mul_f32_e32 v107, 0xbfb8aa3b, v101
	v_mul_f32_e32 v108, 0xbfb8aa3b, v84
	v_mul_f32_e32 v109, 0xbfb8aa3b, v85
	v_exp_f32_e32 v106, v106
	v_rcp_f32_e32 v8, v67
	v_rcp_f32_e32 v9, v114
	v_exp_f32_e32 v107, v107
	v_exp_f32_e32 v108, v108
	v_exp_f32_e32 v109, v109
	v_add_f32_e32 v118, 1.0, v118
	v_add_f32_e32 v234, 1.0, v234
	v_add_f32_e32 v235, 1.0, v235
	v_add_f32_e32 v115, 1.0, v115
	v_add_f32_e32 v116, 1.0, v116
	v_add_f32_e32 v117, 1.0, v117
	v_add_f32_e32 v249, 1.0, v106
	v_add_f32_e32 v250, 1.0, v107
	v_add_f32_e32 v251, 1.0, v108
	v_add_f32_e32 v179, 1.0, v109
	v_add_f32_e32 v104, 1.0, v119
	v_add_f32_e32 v105, 1.0, v120
	v_add_f32_e32 v119, 1.0, v121
	v_add_f32_e32 v120, 1.0, v122
	v_add_f32_e32 v121, 1.0, v123
	v_add_f32_e32 v122, 1.0, v124
	v_add_f32_e32 v123, 1.0, v125
	v_add_f32_e32 v124, 1.0, v126
	v_add_f32_e32 v125, 1.0, v127
	v_add_f32_e32 v126, 1.0, v128
	v_add_f32_e32 v127, 1.0, v129
	v_add_f32_e32 v128, 1.0, v154
	v_add_f32_e32 v129, 1.0, v155
	v_add_f32_e32 v154, 1.0, v156
	v_add_f32_e32 v155, 1.0, v157
	v_add_f32_e32 v156, 1.0, v158
	v_add_f32_e32 v157, 1.0, v159
	v_add_f32_e32 v158, 1.0, v160
	v_add_f32_e32 v159, 1.0, v161
	v_add_f32_e32 v160, 1.0, v162
	v_add_f32_e32 v161, 1.0, v163
	v_add_f32_e32 v162, 1.0, v164
	v_rcp_f32_e32 v103, v118
	v_rcp_f32_e32 v106, v119
	v_rcp_f32_e32 v118, v161
	v_rcp_f32_e32 v119, v162
	v_rcp_f32_e32 v161, v234
	v_rcp_f32_e32 v162, v235
	v_pk_mul_f32 v[234:235], v[8:9], v[22:23]
	v_add_f32_e32 v163, 1.0, v165
	v_add_f32_e32 v164, 1.0, v168
	v_add_f32_e32 v165, 1.0, v169
	v_add_f32_e32 v168, 1.0, v170
	v_add_f32_e32 v169, 1.0, v98
	v_add_f32_e32 v170, 1.0, v99
	v_rcp_f32_e32 v98, v115
	v_rcp_f32_e32 v99, v116
	v_rcp_f32_e32 v102, v117
	v_rcp_f32_e32 v104, v104
	v_rcp_f32_e32 v105, v105
	v_rcp_f32_e32 v107, v120
	v_rcp_f32_e32 v108, v121
	v_rcp_f32_e32 v109, v122
	v_rcp_f32_e32 v110, v123
	v_rcp_f32_e32 v111, v124
	v_rcp_f32_e32 v112, v125
	v_rcp_f32_e32 v113, v126
	v_rcp_f32_e32 v114, v127
	v_rcp_f32_e32 v115, v128
	v_rcp_f32_e32 v116, v129
	v_rcp_f32_e32 v117, v154
	v_add_f32_e32 v171, 1.0, v171
	v_add_f32_e32 v208, 1.0, v208
	v_add_f32_e32 v209, 1.0, v209
	v_add_f32_e32 v210, 1.0, v210
	v_add_f32_e32 v211, 1.0, v211
	v_add_f32_e32 v212, 1.0, v212
	v_add_f32_e32 v213, 1.0, v213
	v_add_f32_e32 v214, 1.0, v214
	v_add_f32_e32 v215, 1.0, v215
	v_add_f32_e32 v232, 1.0, v232
	v_add_f32_e32 v233, 1.0, v233
	v_add_f32_e32 v236, 1.0, v236
	v_add_f32_e32 v237, 1.0, v237
	v_add_f32_e32 v238, 1.0, v238
	v_add_f32_e32 v239, 1.0, v239
	v_add_f32_e32 v240, 1.0, v240
	v_add_f32_e32 v241, 1.0, v241
	v_add_f32_e32 v242, 1.0, v242
	v_add_f32_e32 v243, 1.0, v243
	v_add_f32_e32 v244, 1.0, v244
	v_pk_mul_f32 v[98:99], v[98:99], v[24:25]
	v_pk_mul_f32 v[102:103], v[102:103], v[26:27]
	v_pk_mul_f32 v[104:105], v[104:105], v[28:29]
	v_pk_mul_f32 v[106:107], v[106:107], v[34:35]
	v_pk_mul_f32 v[108:109], v[108:109], v[36:37]
	v_pk_mul_f32 v[110:111], v[110:111], v[38:39]
	v_pk_mul_f32 v[112:113], v[112:113], v[40:41]
	v_rcp_f32_e32 v10, v155
	v_rcp_f32_e32 v11, v156
	v_rcp_f32_e32 v12, v157
	v_rcp_f32_e32 v13, v158
	v_pk_mul_f32 v[114:115], v[114:115], v[42:43]
	v_pk_mul_f32 v[46:47], v[10:11], v[46:47]
	v_pk_mul_f32 v[116:117], v[116:117], v[44:45]
	v_pk_mul_f32 v[48:49], v[12:13], v[48:49]
	v_rcp_f32_e32 v68, v159
	v_rcp_f32_e32 v69, v160
	v_rcp_f32_e32 v120, v163
	v_rcp_f32_e32 v121, v164
	v_rcp_f32_e32 v122, v165
	v_rcp_f32_e32 v123, v168
	v_rcp_f32_e32 v124, v169
	v_rcp_f32_e32 v125, v170
	v_rcp_f32_e32 v126, v171
	v_rcp_f32_e32 v127, v208
	v_rcp_f32_e32 v128, v209
	v_rcp_f32_e32 v129, v210
	v_rcp_f32_e32 v154, v211
	v_rcp_f32_e32 v155, v212
	v_rcp_f32_e32 v156, v213
	v_rcp_f32_e32 v157, v214
	v_rcp_f32_e32 v158, v215
	v_rcp_f32_e32 v159, v232
	v_rcp_f32_e32 v160, v233
	v_rcp_f32_e32 v163, v236
	v_rcp_f32_e32 v164, v245
	v_rcp_f32_e32 v165, v246
	v_rcp_f32_e32 v168, v237
	v_rcp_f32_e32 v169, v238
	v_rcp_f32_e32 v170, v239
	v_rcp_f32_e32 v171, v240
	v_rcp_f32_e32 v208, v241
	v_rcp_f32_e32 v209, v242
	v_rcp_f32_e32 v210, v247
	v_rcp_f32_e32 v211, v248
	v_rcp_f32_e32 v212, v243
	v_rcp_f32_e32 v213, v244
	v_rcp_f32_e32 v214, v249
	v_rcp_f32_e32 v215, v250
	v_rcp_f32_e32 v232, v251
	v_rcp_f32_e32 v233, v179
	v_pk_mul_f32 v[50:51], v[68:69], v[50:51]
	v_pk_mul_f32 v[52:53], v[118:119], v[52:53]
	v_pk_mul_f32 v[54:55], v[120:121], v[54:55]
	v_pk_mul_f32 v[56:57], v[122:123], v[56:57]
	v_pk_mul_f32 v[58:59], v[124:125], v[58:59]
	v_pk_mul_f32 v[62:63], v[126:127], v[62:63]
	v_pk_mul_f32 v[64:65], v[128:129], v[64:65]
	v_pk_mul_f32 v[68:69], v[154:155], v[70:71]
	v_pk_mul_f32 v[70:71], v[156:157], v[72:73]
	v_pk_mul_f32 v[72:73], v[158:159], v[76:77]
	v_pk_mul_f32 v[76:77], v[160:161], v[78:79]
	v_pk_mul_f32 v[78:79], v[162:163], v[80:81]
	v_pk_mul_f32 v[80:81], v[164:165], v[90:91]
	v_pk_mul_f32 v[86:87], v[168:169], v[86:87]
	v_pk_mul_f32 v[90:91], v[170:171], v[92:93]
	v_pk_mul_f32 v[88:89], v[208:209], v[88:89]
	v_pk_mul_f32 v[92:93], v[210:211], v[94:95]
	v_pk_mul_f32 v[94:95], v[212:213], v[96:97]
	v_pk_mul_f32 v[96:97], v[214:215], v[100:101]
	v_pk_mul_f32 v[84:85], v[232:233], v[84:85]
	s_waitcnt lgkmcnt(0)
	s_barrier
	ds_read_b128 v[4:7], v223
	ds_read_b128 v[8:11], v224
	ds_read_b128 v[12:15], v225
	ds_read_b128 v[22:25], v226
	ds_read_b128 v[26:29], v227
	ds_read_b128 v[34:37], v228
	ds_read_b128 v[38:41], v229
	ds_read_b128 v[42:45], v230
	s_waitcnt lgkmcnt(7)
	v_lshlrev_b32_e32 v16, 16, v4
	v_and_b32_e32 v17, 0xffff0000, v4
	v_lshlrev_b32_e32 v4, 16, v5
	v_and_b32_e32 v5, 0xffff0000, v5
	v_lshlrev_b32_e32 v66, 16, v6
	v_and_b32_e32 v67, 0xffff0000, v6
	v_lshlrev_b32_e32 v6, 16, v7
	v_and_b32_e32 v7, 0xffff0000, v7
	s_waitcnt lgkmcnt(6)
	v_lshlrev_b32_e32 v100, 16, v8
	v_and_b32_e32 v101, 0xffff0000, v8
	v_lshlrev_b32_e32 v8, 16, v9
	v_and_b32_e32 v9, 0xffff0000, v9
	v_lshlrev_b32_e32 v118, 16, v10
	v_and_b32_e32 v119, 0xffff0000, v10
	v_lshlrev_b32_e32 v10, 16, v11
	v_and_b32_e32 v11, 0xffff0000, v11
	s_waitcnt lgkmcnt(5)
	v_lshlrev_b32_e32 v120, 16, v12
	v_and_b32_e32 v121, 0xffff0000, v12
	v_lshlrev_b32_e32 v12, 16, v13
	v_and_b32_e32 v13, 0xffff0000, v13
	v_lshlrev_b32_e32 v122, 16, v14
	v_and_b32_e32 v123, 0xffff0000, v14
	v_lshlrev_b32_e32 v14, 16, v15
	v_and_b32_e32 v15, 0xffff0000, v15
	s_waitcnt lgkmcnt(4)
	v_lshlrev_b32_e32 v124, 16, v22
	v_and_b32_e32 v125, 0xffff0000, v22
	v_lshlrev_b32_e32 v22, 16, v23
	v_and_b32_e32 v23, 0xffff0000, v23
	v_lshlrev_b32_e32 v126, 16, v24
	v_and_b32_e32 v127, 0xffff0000, v24
	v_lshlrev_b32_e32 v24, 16, v25
	v_and_b32_e32 v25, 0xffff0000, v25
	s_waitcnt lgkmcnt(3)
	v_lshlrev_b32_e32 v128, 16, v26
	v_and_b32_e32 v129, 0xffff0000, v26
	v_lshlrev_b32_e32 v26, 16, v27
	v_and_b32_e32 v27, 0xffff0000, v27
	v_lshlrev_b32_e32 v154, 16, v28
	v_and_b32_e32 v155, 0xffff0000, v28
	v_lshlrev_b32_e32 v28, 16, v29
	v_and_b32_e32 v29, 0xffff0000, v29
	s_waitcnt lgkmcnt(2)
	v_lshlrev_b32_e32 v156, 16, v34
	v_and_b32_e32 v157, 0xffff0000, v34
	v_lshlrev_b32_e32 v34, 16, v35
	v_and_b32_e32 v35, 0xffff0000, v35
	v_lshlrev_b32_e32 v158, 16, v36
	v_and_b32_e32 v159, 0xffff0000, v36
	v_lshlrev_b32_e32 v36, 16, v37
	v_and_b32_e32 v37, 0xffff0000, v37
	s_waitcnt lgkmcnt(1)
	v_lshlrev_b32_e32 v160, 16, v38
	v_and_b32_e32 v161, 0xffff0000, v38
	v_lshlrev_b32_e32 v38, 16, v39
	v_and_b32_e32 v39, 0xffff0000, v39
	v_lshlrev_b32_e32 v162, 16, v40
	v_and_b32_e32 v163, 0xffff0000, v40
	v_lshlrev_b32_e32 v40, 16, v41
	v_and_b32_e32 v41, 0xffff0000, v41
	s_waitcnt lgkmcnt(0)
	v_lshlrev_b32_e32 v164, 16, v42
	v_and_b32_e32 v165, 0xffff0000, v42
	v_lshlrev_b32_e32 v42, 16, v43
	v_and_b32_e32 v43, 0xffff0000, v43
	v_lshlrev_b32_e32 v168, 16, v44
	v_and_b32_e32 v169, 0xffff0000, v44
	v_lshlrev_b32_e32 v44, 16, v45
	v_and_b32_e32 v45, 0xffff0000, v45
	v_pk_mul_f32 v[16:17], v[234:235], v[16:17]
	v_pk_mul_f32 v[98:99], v[98:99], v[4:5]
	v_pk_mul_f32 v[66:67], v[102:103], v[66:67]
	v_pk_mul_f32 v[102:103], v[104:105], v[6:7]
	v_pk_mul_f32 v[100:101], v[106:107], v[100:101]
	v_pk_mul_f32 v[104:105], v[108:109], v[8:9]
	v_pk_mul_f32 v[106:107], v[110:111], v[118:119]
	v_pk_mul_f32 v[108:109], v[112:113], v[10:11]
	v_pk_mul_f32 v[110:111], v[114:115], v[120:121]
	v_pk_mul_f32 v[112:113], v[116:117], v[12:13]
	v_pk_mul_f32 v[46:47], v[46:47], v[122:123]
	v_pk_mul_f32 v[48:49], v[48:49], v[14:15]
	v_pk_mul_f32 v[50:51], v[50:51], v[124:125]
	v_pk_mul_f32 v[52:53], v[52:53], v[22:23]
	v_pk_mul_f32 v[54:55], v[54:55], v[126:127]
	v_pk_mul_f32 v[56:57], v[56:57], v[24:25]
	v_pk_mul_f32 v[58:59], v[58:59], v[128:129]
	v_pk_mul_f32 v[62:63], v[62:63], v[26:27]
	v_pk_mul_f32 v[64:65], v[64:65], v[154:155]
	v_pk_mul_f32 v[68:69], v[68:69], v[28:29]
	v_pk_mul_f32 v[70:71], v[70:71], v[156:157]
	v_pk_mul_f32 v[72:73], v[72:73], v[34:35]
	v_pk_mul_f32 v[76:77], v[76:77], v[158:159]
	v_pk_mul_f32 v[78:79], v[78:79], v[36:37]
	v_pk_mul_f32 v[80:81], v[80:81], v[160:161]
	v_pk_mul_f32 v[86:87], v[86:87], v[38:39]
	v_pk_mul_f32 v[90:91], v[90:91], v[162:163]
	v_pk_mul_f32 v[88:89], v[88:89], v[40:41]
	v_pk_mul_f32 v[92:93], v[92:93], v[164:165]
	v_pk_mul_f32 v[94:95], v[94:95], v[42:43]
	v_pk_mul_f32 v[96:97], v[96:97], v[168:169]
	v_pk_mul_f32 v[84:85], v[84:85], v[44:45]
	v_cvt_pk_bf16_f32 v4, v16, v17
	v_cvt_pk_bf16_f32 v5, v98, v99
	v_cvt_pk_bf16_f32 v6, v66, v67
	v_cvt_pk_bf16_f32 v7, v102, v103
	v_cvt_pk_bf16_f32 v8, v100, v101
	v_cvt_pk_bf16_f32 v9, v104, v105
	v_cvt_pk_bf16_f32 v10, v106, v107
	v_cvt_pk_bf16_f32 v11, v108, v109
	v_cvt_pk_bf16_f32 v12, v110, v111
	v_cvt_pk_bf16_f32 v13, v112, v113
	v_cvt_pk_bf16_f32 v14, v46, v47
	v_cvt_pk_bf16_f32 v15, v48, v49
	v_cvt_pk_bf16_f32 v22, v50, v51
	v_cvt_pk_bf16_f32 v23, v52, v53
	v_cvt_pk_bf16_f32 v24, v54, v55
	v_cvt_pk_bf16_f32 v25, v56, v57
	v_cvt_pk_bf16_f32 v26, v58, v59
	v_cvt_pk_bf16_f32 v27, v62, v63
	v_cvt_pk_bf16_f32 v28, v64, v65
	v_cvt_pk_bf16_f32 v29, v68, v69
	v_cvt_pk_bf16_f32 v34, v70, v71
	v_cvt_pk_bf16_f32 v35, v72, v73
	v_cvt_pk_bf16_f32 v36, v76, v77
	v_cvt_pk_bf16_f32 v37, v78, v79
	v_cvt_pk_bf16_f32 v38, v80, v81
	v_cvt_pk_bf16_f32 v39, v86, v87
	v_cvt_pk_bf16_f32 v40, v90, v91
	v_cvt_pk_bf16_f32 v41, v88, v89
	v_cvt_pk_bf16_f32 v42, v92, v93
	v_cvt_pk_bf16_f32 v43, v94, v95
	v_cvt_pk_bf16_f32 v44, v96, v97
	v_cvt_pk_bf16_f32 v45, v84, v85
	global_store_dwordx4 v[18:19], v[4:7], off
	global_store_dwordx4 v[20:21], v[8:11], off
	global_store_dwordx4 v[30:31], v[12:15], off
	global_store_dwordx4 v[32:33], v[22:25], off
	global_store_dwordx4 v[60:61], v[26:29], off
	global_store_dwordx4 v[74:75], v[34:37], off
	global_store_dwordx4 v[82:83], v[38:41], off
	global_store_dwordx4 v[2:3], v[42:45], off
	s_waitcnt lgkmcnt(0)
	s_barrier

.LBB0_1413:
	s_and_saveexec_b64 s[0:1], s[40:41]
	s_cbranch_execz .LBB0_1417
	s_waitcnt vmcnt(0)
	v_mov_b32_e32 v3, s80
	ds_write_b32 v3, v231

.LBB0_1424:
	s_lshl_b32 s0, s91, 14
	s_add_i32 s38, s0, 0
	s_add_i32 s39, s91, 0x680
	s_add_i32 s49, s91, 0x688
	s_add_u32 s0, s46, 0x1900000
	s_addc_u32 s1, s47, 0
	s_add_u32 s4, s46, 0x1100000
	s_addc_u32 s5, s47, 0
	s_add_u32 s6, s46, 0x900000
	s_addc_u32 s7, s47, 0
	s_add_u32 s8, s46, 0x700000
	s_addc_u32 s9, s47, 0
	s_add_u32 s10, s46, 0x1b00000
	s_addc_u32 s11, s47, 0
	s_add_u32 s12, s46, 0x100000
	s_addc_u32 s13, s47, 0
	s_add_i32 s54, 0, 0x27e50
	v_mov_b32_e32 v17, 0
	v_mov_b32_e32 v1, s54
	s_add_i32 s55, 0, 0x27ef8
	s_add_i32 s74, 0, 0x27efc
	s_add_i32 s75, 0, 0x27ef0
	s_add_i32 s76, 0, 0x27ef4
	s_add_i32 s77, 0, 0x27ee8
	s_add_i32 s78, 0, 0x27eec
	s_add_i32 s79, 0, 0x27ee0
	s_add_i32 s80, 0, 0x27ee4
	s_add_i32 s81, 0, 0x27ed8
	s_add_i32 s82, 0, 0x27edc
	s_add_i32 s83, 0, 0x27ed0
	s_add_i32 s84, 0, 0x27ed4
	s_add_i32 s85, 0, 0x27f00
	s_add_i32 s92, 0, 0x27f04
	s_add_i32 s93, 0, 0x27ea0
	s_add_i32 s94, 0, 0x27ea4
	s_add_i32 s95, 0, 0x27e98
	s_add_i32 s96, 0, 0x27e9c
	s_movk_i32 s97, 0x7fff
	s_mov_b32 s88, 0xffff0000
	v_and_b32_e32 v248, 63, v0
	s_and_saveexec_b64 s[98:99], s[40:41]
	v_mov_b32_e32 v231, 1
	global_atomic_add v231, v17, v231, s[46:47] offset:384 sc0
	s_mov_b64 exec, s[98:99]
	s_branch .LBB0_1428

.LBB0_1426:
	s_movk_i32 s19, 0x84
	v_lshlrev_b32_e32 v16, 2, v27
	v_mul_lo_u32 v25, v28, s19
	v_add3_u32 v16, s38, v16, v25
	v_add_u32_e32 v93, 0x400, v16
	v_add_u32_e32 v94, 0x800, v16
	v_add_u32_e32 v95, 0xc00, v16
	v_add_u32_e32 v96, 0x1000, v16
	s_waitcnt vmcnt(0) lgkmcnt(0)
	s_and_saveexec_b64 s[98:99], s[40:41]
	v_mov_b32_e32 v231, 1
	global_atomic_add v231, v17, v231, s[46:47] offset:384 sc0
	s_mov_b64 exec, s[98:99]
	ds_write2_b32 v16, v29, v30 offset1:66
	ds_write2_b32 v16, v31, v33 offset0:132 offset1:198
	ds_write2_b32 v93, v32, v34 offset0:8 offset1:74
	ds_write2_b32 v93, v35, v36 offset0:140 offset1:206
	ds_write2_b32 v94, v37, v38 offset0:16 offset1:82
	ds_write2_b32 v94, v39, v40 offset0:148 offset1:214
	ds_write2_b32 v95, v41, v42 offset0:24 offset1:90
	ds_write2_b32 v95, v43, v44 offset0:156 offset1:222
	ds_write2_b32 v96, v45, v46 offset0:32 offset1:98
	ds_write2_b32 v96, v47, v48 offset0:164 offset1:230
	v_add_u32_e32 v48, 0x1400, v16
	ds_write2_b32 v48, v49, v50 offset0:40 offset1:106
	ds_write2_b32 v48, v51, v52 offset0:172 offset1:238
	v_add_u32_e32 v49, 0x1800, v16
	v_add_u32_e32 v50, 0x1c00, v16
	ds_write2_b32 v49, v53, v54 offset0:48 offset1:114
	ds_write2_b32 v49, v55, v56 offset0:180 offset1:246
	ds_write2_b32 v50, v57, v58 offset0:56 offset1:122
	ds_write2_b32 v50, v59, v60 offset0:188 offset1:254
	v_ashrrev_i32_e32 v51, 3, v26
	s_waitcnt lgkmcnt(0)
	v_mul_u32_u24_e32 v24, 0x84, v24
	v_lshlrev_b32_e32 v25, 2, v51
	v_add3_u32 v52, s38, v24, v25
	ds_read2_b32 v[28:29], v52 offset1:8
	ds_read2_b32 v[30:31], v52 offset0:66 offset1:74
	ds_read2_b32 v[32:33], v52 offset0:33 offset1:41
	ds_read2_b32 v[34:35], v52 offset0:99 offset1:107
	ds_read2_b32 v[36:37], v52 offset0:132 offset1:140
	ds_read2_b32 v[38:39], v52 offset0:198 offset1:206
	ds_read2_b32 v[40:41], v52 offset0:165 offset1:173
	ds_read2_b32 v[42:43], v52 offset0:231 offset1:239
	s_waitcnt lgkmcnt(7)
	v_mov_b32_e32 v24, v28
	s_waitcnt lgkmcnt(5)
	v_mov_b32_e32 v26, v32
	s_waitcnt lgkmcnt(4)
	v_mov_b32_e32 v27, v34
	s_waitcnt lgkmcnt(3)
	v_mov_b32_e32 v44, v36
	s_waitcnt lgkmcnt(2)
	v_mov_b32_e32 v45, v38
	s_waitcnt lgkmcnt(1)
	v_mov_b32_e32 v46, v40
	s_waitcnt lgkmcnt(0)
	v_mov_b32_e32 v47, v42
	v_mov_b32_e32 v25, v30
	v_pk_mul_f32 v[26:27], v[18:19], v[26:27]
	v_pk_mul_f32 v[44:45], v[6:7], v[44:45]
	v_pk_mul_f32 v[46:47], v[4:5], v[46:47]
	v_pk_mul_f32 v[24:25], v[2:3], v[24:25]
	v_bfe_u32 v28, v47, 16, 1
	v_bfe_u32 v32, v27, 16, 1
	v_bfe_u32 v36, v44, 16, 1
	v_bfe_u32 v30, v46, 16, 1
	v_bfe_u32 v34, v26, 16, 1
	v_add3_u32 v32, v27, v32, s97
	v_add3_u32 v27, v47, v28, s97
	v_bfe_u32 v28, v24, 16, 1
	v_bfe_u32 v38, v45, 16, 1
	v_add3_u32 v36, v44, v36, s97
	v_add3_u32 v34, v26, v34, s97
	v_add3_u32 v26, v46, v30, s97
	v_bfe_u32 v30, v25, 16, 1
	v_add3_u32 v38, v45, v38, s97
	v_add3_u32 v24, v24, v28, s97
	v_lshrrev_b32_e32 v28, 16, v36
	v_add3_u32 v25, v25, v30, s97
	v_lshrrev_b32_e32 v30, 16, v38
	v_and_or_b32 v26, v26, s88, v28
	v_add_u32_e32 v28, s33, v51
	v_lshrrev_b32_e32 v25, 16, v25
	v_and_or_b32 v27, v27, s88, v30
	v_ashrrev_i32_e32 v30, 31, v28
	v_and_or_b32 v25, v32, s88, v25
	v_mul_lo_u32 v30, s14, v30
	v_mul_lo_u32 v32, s15, v28
	v_mad_u64_u32 v[44:45], s[24:25], s14, v28, 0
	v_add3_u32 v45, v45, v30, v32
	s_ashr_i32 s19, s18, 31
	v_lshl_add_u64 v[44:45], v[44:45], 1, s[16:17]
	s_lshl_b64 s[18:19], s[18:19], 1
	v_lshrrev_b32_e32 v24, 16, v24
	v_lshl_add_u64 v[44:45], v[44:45], 0, s[18:19]
	v_lshlrev_b64 v[12:13], 1, v[12:13]
	v_and_or_b32 v24, v34, s88, v24
	v_lshl_add_u64 v[44:45], v[44:45], 0, v[12:13]
	v_mov_b32_e32 v30, v29
	v_mov_b32_e32 v34, v33
	v_mov_b32_e32 v42, v41
	global_store_dwordx4 v[44:45], v[24:27], off sc1
	v_mov_b32_e32 v38, v37
	v_pk_mul_f32 v[28:29], v[6:7], v[38:39]
	v_pk_mul_f32 v[24:25], v[2:3], v[30:31]
	v_pk_mul_f32 v[26:27], v[18:19], v[34:35]
	v_pk_mul_f32 v[30:31], v[4:5], v[42:43]
	v_bfe_u32 v34, v27, 16, 1
	v_bfe_u32 v32, v31, 16, 1
	v_bfe_u32 v33, v30, 16, 1
	v_bfe_u32 v35, v26, 16, 1
	v_add3_u32 v34, v27, v34, s97
	v_add3_u32 v27, v31, v32, s97
	v_bfe_u32 v32, v28, 16, 1
	v_add3_u32 v35, v26, v35, s97
	v_add3_u32 v26, v30, v33, s97
	v_bfe_u32 v33, v29, 16, 1
	v_add3_u32 v28, v28, v32, s97
	v_add_u32_e32 v53, 8, v51
	v_add3_u32 v29, v29, v33, s97
	v_lshrrev_b32_e32 v28, 16, v28
	v_lshrrev_b32_e32 v29, 16, v29
	v_and_or_b32 v26, v26, s88, v28
	v_add_u32_e32 v28, s33, v53
	v_bfe_u32 v30, v24, 16, 1
	v_bfe_u32 v31, v25, 16, 1
	v_and_or_b32 v27, v27, s88, v29
	v_ashrrev_i32_e32 v29, 31, v28
	v_add3_u32 v25, v25, v31, s97
	v_add3_u32 v24, v24, v30, s97
	v_mul_lo_u32 v30, s14, v29
	v_mul_lo_u32 v31, s15, v28
	v_mad_u64_u32 v[28:29], s[24:25], s14, v28, 0
	v_add3_u32 v29, v29, v30, v31
	v_lshl_add_u64 v[28:29], v[28:29], 1, s[16:17]
	v_lshrrev_b32_e32 v24, 16, v24
	v_lshrrev_b32_e32 v25, 16, v25
	v_lshl_add_u64 v[28:29], v[28:29], 0, s[18:19]
	v_and_or_b32 v25, v34, s88, v25
	v_and_or_b32 v24, v35, s88, v24
	v_lshl_add_u64 v[28:29], v[28:29], 0, v[12:13]
	global_store_dwordx4 v[28:29], v[24:27], off sc1
	ds_read2_b32 v[28:29], v52 offset0:16 offset1:24
	ds_read2_b32 v[30:31], v52 offset0:82 offset1:90
	ds_read2_b32 v[32:33], v52 offset0:49 offset1:57
	ds_read2_b32 v[34:35], v52 offset0:115 offset1:123
	ds_read2_b32 v[36:37], v52 offset0:148 offset1:156
	ds_read2_b32 v[38:39], v52 offset0:214 offset1:222
	ds_read2_b32 v[40:41], v52 offset0:181 offset1:189
	ds_read2_b32 v[42:43], v52 offset0:247 offset1:255
	s_waitcnt lgkmcnt(7)
	v_mov_b32_e32 v24, v28
	s_waitcnt lgkmcnt(5)
	v_mov_b32_e32 v26, v32
	s_waitcnt lgkmcnt(4)
	v_mov_b32_e32 v27, v34
	s_waitcnt lgkmcnt(3)
	v_mov_b32_e32 v44, v36
	s_waitcnt lgkmcnt(2)
	v_mov_b32_e32 v45, v38
	s_waitcnt lgkmcnt(1)
	v_mov_b32_e32 v46, v40
	s_waitcnt lgkmcnt(0)
	v_mov_b32_e32 v47, v42
	v_mov_b32_e32 v25, v30
	v_pk_mul_f32 v[26:27], v[18:19], v[26:27]
	v_pk_mul_f32 v[44:45], v[6:7], v[44:45]
	v_pk_mul_f32 v[46:47], v[4:5], v[46:47]
	v_pk_mul_f32 v[24:25], v[2:3], v[24:25]
	v_bfe_u32 v28, v47, 16, 1
	v_bfe_u32 v32, v27, 16, 1
	v_bfe_u32 v36, v44, 16, 1
	v_bfe_u32 v30, v46, 16, 1
	v_bfe_u32 v34, v26, 16, 1
	v_add3_u32 v32, v27, v32, s97
	v_add3_u32 v27, v47, v28, s97
	v_bfe_u32 v28, v24, 16, 1
	v_bfe_u32 v38, v45, 16, 1
	v_add3_u32 v36, v44, v36, s97
	v_add_u32_e32 v54, 16, v51
	v_add3_u32 v34, v26, v34, s97
	v_add3_u32 v26, v46, v30, s97
	v_bfe_u32 v30, v25, 16, 1
	v_add3_u32 v38, v45, v38, s97
	v_add3_u32 v24, v24, v28, s97
	v_lshrrev_b32_e32 v28, 16, v36
	v_add3_u32 v25, v25, v30, s97
	v_lshrrev_b32_e32 v30, 16, v38
	v_and_or_b32 v26, v26, s88, v28
	v_add_u32_e32 v28, s33, v54
	v_lshrrev_b32_e32 v25, 16, v25
	v_and_or_b32 v27, v27, s88, v30
	v_ashrrev_i32_e32 v30, 31, v28
	v_and_or_b32 v25, v32, s88, v25
	v_mul_lo_u32 v30, s14, v30
	v_mul_lo_u32 v32, s15, v28
	v_mad_u64_u32 v[44:45], s[24:25], s14, v28, 0
	v_add3_u32 v45, v45, v30, v32
	v_lshrrev_b32_e32 v24, 16, v24
	v_lshl_add_u64 v[44:45], v[44:45], 1, s[16:17]
	v_and_or_b32 v24, v34, s88, v24
	v_lshl_add_u64 v[44:45], v[44:45], 0, s[18:19]
	v_mov_b32_e32 v34, v33
	v_lshl_add_u64 v[44:45], v[44:45], 0, v[12:13]
	v_pk_mul_f32 v[18:19], v[18:19], v[34:35]
	v_mov_b32_e32 v38, v37
	global_store_dwordx4 v[44:45], v[24:27], off sc1
	v_pk_mul_f32 v[6:7], v[6:7], v[38:39]
	v_mov_b32_e32 v42, v41
	v_bfe_u32 v26, v19, 16, 1
	v_mov_b32_e32 v30, v29
	v_pk_mul_f32 v[4:5], v[4:5], v[42:43]
	v_bfe_u32 v27, v18, 16, 1
	v_add3_u32 v19, v19, v26, s97
	v_bfe_u32 v26, v6, 16, 1
	v_pk_mul_f32 v[2:3], v[2:3], v[30:31]
	v_bfe_u32 v24, v5, 16, 1
	v_bfe_u32 v25, v4, 16, 1
	v_add3_u32 v18, v18, v27, s97
	v_bfe_u32 v27, v7, 16, 1
	v_add3_u32 v6, v6, v26, s97
	v_add_u32_e32 v40, 24, v51
	v_add3_u32 v4, v4, v25, s97
	v_add3_u32 v5, v5, v24, s97
	v_bfe_u32 v24, v2, 16, 1
	v_bfe_u32 v25, v3, 16, 1
	v_add3_u32 v7, v7, v27, s97
	v_lshrrev_b32_e32 v6, 16, v6
	v_add3_u32 v3, v3, v25, s97
	v_add3_u32 v2, v2, v24, s97
	v_lshrrev_b32_e32 v7, 16, v7
	v_and_or_b32 v4, v4, s88, v6
	v_add_u32_e32 v6, s33, v40
	v_lshrrev_b32_e32 v2, 16, v2
	v_lshrrev_b32_e32 v3, 16, v3
	v_and_or_b32 v5, v5, s88, v7
	v_ashrrev_i32_e32 v7, 31, v6
	v_and_or_b32 v3, v19, s88, v3
	v_and_or_b32 v2, v18, s88, v2
	v_mul_lo_u32 v18, s14, v7
	v_mul_lo_u32 v19, s15, v6
	v_mad_u64_u32 v[6:7], s[14:15], s14, v6, 0
	v_add3_u32 v7, v7, v18, v19
	v_lshl_add_u64 v[6:7], v[6:7], 1, s[16:17]
	v_lshl_add_u64 v[6:7], v[6:7], 0, s[18:19]
	v_lshl_add_u64 v[6:7], v[6:7], 0, v[12:13]
	global_store_dwordx4 v[6:7], v[2:5], off sc1
	s_waitcnt lgkmcnt(0)
	ds_write2_b32 v16, v61, v62 offset1:66
	ds_write2_b32 v16, v63, v64 offset0:132 offset1:198
	ds_write2_b32 v93, v65, v66 offset0:8 offset1:74
	ds_write2_b32 v93, v67, v68 offset0:140 offset1:206
	ds_write2_b32 v94, v69, v70 offset0:16 offset1:82
	ds_write2_b32 v94, v71, v72 offset0:148 offset1:214
	ds_write2_b32 v95, v73, v74 offset0:24 offset1:90
	ds_write2_b32 v95, v75, v76 offset0:156 offset1:222
	ds_write2_b32 v96, v77, v78 offset0:32 offset1:98
	ds_write2_b32 v96, v79, v80 offset0:164 offset1:230
	ds_write2_b32 v48, v81, v82 offset0:40 offset1:106
	ds_write2_b32 v48, v83, v84 offset0:172 offset1:238
	ds_write2_b32 v49, v85, v86 offset0:48 offset1:114
	ds_write2_b32 v49, v87, v88 offset0:180 offset1:246
	ds_write2_b32 v50, v89, v90 offset0:56 offset1:122
	ds_write2_b32 v50, v91, v92 offset0:188 offset1:254
	s_waitcnt lgkmcnt(0)
	ds_read2_b32 v[6:7], v52 offset1:8
	ds_read2_b32 v[18:19], v52 offset0:66 offset1:74
	ds_read2_b32 v[24:25], v52 offset0:33 offset1:41
	ds_read2_b32 v[26:27], v52 offset0:99 offset1:107
	ds_read2_b32 v[28:29], v52 offset0:132 offset1:140
	ds_read2_b32 v[30:31], v52 offset0:198 offset1:206
	ds_read2_b32 v[32:33], v52 offset0:165 offset1:173
	ds_read2_b32 v[34:35], v52 offset0:231 offset1:239
	s_waitcnt lgkmcnt(7)
	v_mov_b32_e32 v2, v6
	s_waitcnt lgkmcnt(5)
	v_mov_b32_e32 v4, v24
	s_waitcnt lgkmcnt(4)
	v_mov_b32_e32 v5, v26
	s_waitcnt lgkmcnt(3)
	v_mov_b32_e32 v36, v28
	s_waitcnt lgkmcnt(2)
	v_mov_b32_e32 v37, v30
	s_waitcnt lgkmcnt(1)
	v_mov_b32_e32 v38, v32
	s_waitcnt lgkmcnt(0)
	v_mov_b32_e32 v39, v34
	v_mov_b32_e32 v3, v18
	v_pk_mul_f32 v[4:5], v[14:15], v[4:5]
	v_pk_mul_f32 v[36:37], v[20:21], v[36:37]
	v_pk_mul_f32 v[38:39], v[10:11], v[38:39]
	v_pk_mul_f32 v[2:3], v[8:9], v[2:3]
	v_bfe_u32 v6, v39, 16, 1
	v_bfe_u32 v18, v5, 16, 1
	v_bfe_u32 v26, v36, 16, 1
	v_bfe_u32 v16, v38, 16, 1
	v_bfe_u32 v24, v4, 16, 1
	v_add3_u32 v18, v5, v18, s97
	v_add3_u32 v5, v39, v6, s97
	v_bfe_u32 v6, v2, 16, 1
	v_bfe_u32 v28, v37, 16, 1
	v_add3_u32 v26, v36, v26, s97
	v_add3_u32 v24, v4, v24, s97
	v_add3_u32 v4, v38, v16, s97
	v_bfe_u32 v16, v3, 16, 1
	v_add3_u32 v28, v37, v28, s97
	v_add3_u32 v2, v2, v6, s97
	v_lshrrev_b32_e32 v6, 16, v26
	v_add3_u32 v3, v3, v16, s97
	v_lshrrev_b32_e32 v16, 16, v28
	v_and_or_b32 v4, v4, s88, v6
	v_add_u32_e32 v6, s90, v51
	v_lshrrev_b32_e32 v3, 16, v3
	v_and_or_b32 v5, v5, s88, v16
	v_ashrrev_i32_e32 v16, 31, v6
	v_and_or_b32 v3, v18, s88, v3
	v_mul_lo_u32 v16, s20, v16
	v_mul_lo_u32 v18, s21, v6
	v_mad_u64_u32 v[36:37], s[14:15], s20, v6, 0
	v_add3_u32 v37, v37, v16, v18
	v_lshl_add_u64 v[36:37], v[36:37], 1, s[22:23]
	v_lshlrev_b64 v[22:23], 1, v[22:23]
	v_lshrrev_b32_e32 v2, 16, v2
	v_lshl_add_u64 v[36:37], v[36:37], 0, v[22:23]
	v_and_or_b32 v2, v24, s88, v2
	v_lshl_add_u64 v[36:37], v[36:37], 0, v[12:13]
	v_mov_b32_e32 v18, v7
	v_mov_b32_e32 v26, v25
	v_mov_b32_e32 v34, v33
	global_store_dwordx4 v[36:37], v[2:5], off sc1
	v_mov_b32_e32 v30, v29
	v_pk_mul_f32 v[6:7], v[20:21], v[30:31]
	v_pk_mul_f32 v[2:3], v[8:9], v[18:19]
	v_pk_mul_f32 v[4:5], v[14:15], v[26:27]
	v_pk_mul_f32 v[18:19], v[10:11], v[34:35]
	v_bfe_u32 v25, v5, 16, 1
	v_bfe_u32 v16, v19, 16, 1
	v_bfe_u32 v24, v18, 16, 1
	v_bfe_u32 v26, v4, 16, 1
	v_add3_u32 v25, v5, v25, s97
	v_add3_u32 v5, v19, v16, s97
	v_bfe_u32 v19, v6, 16, 1
	v_add3_u32 v26, v4, v26, s97
	v_add3_u32 v4, v18, v24, s97
	v_bfe_u32 v24, v7, 16, 1
	v_add3_u32 v6, v6, v19, s97
	v_add3_u32 v7, v7, v24, s97
	v_lshrrev_b32_e32 v6, 16, v6
	v_lshrrev_b32_e32 v7, 16, v7
	v_and_or_b32 v4, v4, s88, v6
	v_add_u32_e32 v6, s90, v53
	v_bfe_u32 v16, v2, 16, 1
	v_bfe_u32 v18, v3, 16, 1
	v_and_or_b32 v5, v5, s88, v7
	v_ashrrev_i32_e32 v7, 31, v6
	v_add3_u32 v3, v3, v18, s97
	v_add3_u32 v2, v2, v16, s97
	v_mul_lo_u32 v16, s20, v7
	v_mul_lo_u32 v18, s21, v6
	v_mad_u64_u32 v[6:7], s[14:15], s20, v6, 0
	v_add3_u32 v7, v7, v16, v18
	v_lshl_add_u64 v[6:7], v[6:7], 1, s[22:23]
	v_lshrrev_b32_e32 v2, 16, v2
	v_lshrrev_b32_e32 v3, 16, v3
	v_lshl_add_u64 v[6:7], v[6:7], 0, v[22:23]
	v_and_or_b32 v3, v25, s88, v3
	v_and_or_b32 v2, v26, s88, v2
	v_lshl_add_u64 v[6:7], v[6:7], 0, v[12:13]
	ds_read2_b32 v[18:19], v52 offset0:16 offset1:24
	ds_read2_b32 v[24:25], v52 offset0:82 offset1:90
	global_store_dwordx4 v[6:7], v[2:5], off sc1
	ds_read2_b32 v[6:7], v52 offset0:49 offset1:57
	ds_read2_b32 v[26:27], v52 offset0:115 offset1:123
	ds_read2_b32 v[28:29], v52 offset0:148 offset1:156
	ds_read2_b32 v[30:31], v52 offset0:214 offset1:222
	ds_read2_b32 v[32:33], v52 offset0:181 offset1:189
	ds_read2_b32 v[34:35], v52 offset0:247 offset1:255
	s_waitcnt lgkmcnt(7)
	v_mov_b32_e32 v2, v18
	s_waitcnt lgkmcnt(5)
	v_mov_b32_e32 v4, v6
	s_waitcnt lgkmcnt(4)
	v_mov_b32_e32 v5, v26
	s_waitcnt lgkmcnt(3)
	v_mov_b32_e32 v36, v28
	s_waitcnt lgkmcnt(2)
	v_mov_b32_e32 v37, v30
	s_waitcnt lgkmcnt(1)
	v_mov_b32_e32 v38, v32
	s_waitcnt lgkmcnt(0)
	v_mov_b32_e32 v39, v34
	v_mov_b32_e32 v3, v24
	v_pk_mul_f32 v[4:5], v[14:15], v[4:5]
	v_pk_mul_f32 v[36:37], v[20:21], v[36:37]
	v_pk_mul_f32 v[38:39], v[10:11], v[38:39]
	v_pk_mul_f32 v[2:3], v[8:9], v[2:3]
	v_bfe_u32 v6, v39, 16, 1
	v_bfe_u32 v18, v5, 16, 1
	v_bfe_u32 v26, v36, 16, 1
	v_bfe_u32 v16, v38, 16, 1
	v_bfe_u32 v24, v4, 16, 1
	v_add3_u32 v18, v5, v18, s97
	v_add3_u32 v5, v39, v6, s97
	v_bfe_u32 v6, v2, 16, 1
	v_bfe_u32 v28, v37, 16, 1
	v_add3_u32 v26, v36, v26, s97
	v_add3_u32 v24, v4, v24, s97
	v_add3_u32 v4, v38, v16, s97
	v_bfe_u32 v16, v3, 16, 1
	v_add3_u32 v28, v37, v28, s97
	v_add3_u32 v2, v2, v6, s97
	v_lshrrev_b32_e32 v6, 16, v26
	v_add3_u32 v3, v3, v16, s97
	v_lshrrev_b32_e32 v16, 16, v28
	v_and_or_b32 v4, v4, s88, v6
	v_add_u32_e32 v6, s90, v54
	v_lshrrev_b32_e32 v3, 16, v3
	v_and_or_b32 v5, v5, s88, v16
	v_ashrrev_i32_e32 v16, 31, v6
	v_and_or_b32 v3, v18, s88, v3
	v_mul_lo_u32 v16, s20, v16
	v_mul_lo_u32 v18, s21, v6
	v_mad_u64_u32 v[36:37], s[14:15], s20, v6, 0
	v_add3_u32 v37, v37, v16, v18
	v_lshl_add_u64 v[36:37], v[36:37], 1, s[22:23]
	v_lshrrev_b32_e32 v2, 16, v2
	v_lshl_add_u64 v[36:37], v[36:37], 0, v[22:23]
	v_and_or_b32 v2, v24, s88, v2
	v_lshl_add_u64 v[36:37], v[36:37], 0, v[12:13]
	v_mov_b32_e32 v24, v19
	v_mov_b32_e32 v26, v7
	v_mov_b32_e32 v34, v33
	global_store_dwordx4 v[36:37], v[2:5], off sc1
	v_mov_b32_e32 v30, v29
	v_pk_mul_f32 v[6:7], v[20:21], v[30:31]
	v_pk_mul_f32 v[2:3], v[8:9], v[24:25]
	v_pk_mul_f32 v[4:5], v[14:15], v[26:27]
	v_pk_mul_f32 v[8:9], v[10:11], v[34:35]
	v_bfe_u32 v14, v5, 16, 1
	v_bfe_u32 v10, v9, 16, 1
	v_bfe_u32 v11, v8, 16, 1
	v_bfe_u32 v15, v4, 16, 1
	v_add3_u32 v14, v5, v14, s97
	v_add3_u32 v5, v9, v10, s97
	v_bfe_u32 v10, v6, 16, 1
	v_add3_u32 v15, v4, v15, s97
	v_add3_u32 v4, v8, v11, s97
	v_bfe_u32 v11, v7, 16, 1
	v_add3_u32 v6, v6, v10, s97
	v_add3_u32 v7, v7, v11, s97
	v_lshrrev_b32_e32 v6, 16, v6
	v_lshrrev_b32_e32 v7, 16, v7
	v_and_or_b32 v4, v4, s88, v6
	v_add_u32_e32 v6, s90, v40
	v_bfe_u32 v8, v2, 16, 1
	v_bfe_u32 v9, v3, 16, 1
	v_and_or_b32 v5, v5, s88, v7
	v_ashrrev_i32_e32 v7, 31, v6
	v_add3_u32 v3, v3, v9, s97
	v_add3_u32 v2, v2, v8, s97
	v_mul_lo_u32 v8, s20, v7
	v_mul_lo_u32 v9, s21, v6
	v_mad_u64_u32 v[6:7], s[14:15], s20, v6, 0
	v_add3_u32 v7, v7, v8, v9
	v_lshl_add_u64 v[6:7], v[6:7], 1, s[22:23]
	v_lshrrev_b32_e32 v2, 16, v2
	v_lshrrev_b32_e32 v3, 16, v3
	v_lshl_add_u64 v[6:7], v[6:7], 0, v[22:23]
	v_and_or_b32 v3, v14, s88, v3
	v_and_or_b32 v2, v15, s88, v2
	v_lshl_add_u64 v[6:7], v[6:7], 0, v[12:13]
	global_store_dwordx4 v[6:7], v[2:5], off sc1
	s_waitcnt lgkmcnt(0)
	s_mov_b64 s[14:15], 0

.LBB0_1428:
	s_and_saveexec_b64 s[14:15], s[40:41]
	s_cbranch_execz .LBB0_1432
	s_waitcnt vmcnt(0)
	v_mov_b32_e32 v3, s54
	ds_write_b32 v3, v231
